# adj stream loads with sc1 nt instead of nt
# speedup vs baseline: 1.0005x; 1.0005x over previous
_Z11attn_kernelPKfS0_PKDv8_DF16_S0_Pfi:
	s_load_dwordx2 s[28:29], s[0:1], 0x0
	v_cmp_gt_u32_e32 vcc, 8, v0
	s_and_saveexec_b64 s[4:5], vcc
	v_lshlrev_b32_e32 v1, 2, v0
	v_mov_b32_e32 v2, 0
	ds_write_b32 v1, v2 offset:36864
	s_or_b64 exec, exec, s[4:5]
	s_load_dword s33, s[0:1], 0x28
	v_bfe_u32 v1, v0, 6, 2
	v_lshl_or_b32 v82, s2, 2, v1
	v_readfirstlane_b32 s34, v0
	s_cmp_gt_u32 s34, 0xff
	s_cbranch_scc1 .Lsc_early_skip
	v_and_b32_e32 v3, 63, v0
	v_lshlrev_b32_e32 v2, 4, v3
	s_lshr_b32 s35, s34, 6
	s_lshl_b32 s37, s2, 2
	s_add_u32 s37, s37, s35
	s_and_b32 s47, s37, 1
	s_lshl_b32 s47, s47, 2
	s_mul_i32 s38, s37, 0x9c40
	s_lshl_b32 s40, s47, 4
	s_sub_u32 s38, s38, s40
	v_max_u32_e32 v12, s47, v3
	v_lshlrev_b32_e32 v12, 4, v12
	s_waitcnt lgkmcnt(0)
	s_and_b32 s29, s29, 0xffff
	s_mov_b32 s30, 0x17d78400
	s_mov_b32 s31, 0x20000
	buffer_load_dwordx4 v[100:103], v12, s[28:31], s38 offen sc1 nt
	s_add_u32 s40, s38, 0x400
	buffer_load_dwordx4 v[104:107], v2, s[28:31], s40 offen sc1 nt
	s_add_u32 s40, s38, 0x800
	buffer_load_dwordx4 v[108:111], v2, s[28:31], s40 offen sc1 nt
	s_add_u32 s40, s38, 0xc00
	buffer_load_dwordx4 v[112:115], v2, s[28:31], s40 offen sc1 nt
	s_add_u32 s40, s38, 0x1000
	buffer_load_dwordx4 v[116:119], v2, s[28:31], s40 offen sc1 nt
	s_add_u32 s40, s38, 0x1400
	buffer_load_dwordx4 v[120:123], v2, s[28:31], s40 offen sc1 nt
	s_add_u32 s40, s38, 0x1800
	buffer_load_dwordx4 v[124:127], v2, s[28:31], s40 offen sc1 nt
	s_add_u32 s40, s38, 0x1c00
	buffer_load_dwordx4 v[128:131], v2, s[28:31], s40 offen sc1 nt
	s_add_u32 s40, s38, 0x2000
	buffer_load_dwordx4 v[132:135], v2, s[28:31], s40 offen sc1 nt
	s_add_u32 s40, s38, 0x2400
	buffer_load_dwordx4 v[136:139], v2, s[28:31], s40 offen sc1 nt

.Lsc_s0:
	s_add_u32 s40, s38, 0x2800
	buffer_load_dwordx4 v[100:103], v2, s[28:31], s40 offen sc1 nt
	s_waitcnt vmcnt(9)
	v_or3_b32 v12, v104, v105, v106
	v_bitop3_b32 v12, v12, s9, v107 bitop3:0xc8
	v_cmp_ne_u32_e32 vcc, 0, v12
	s_cbranch_vccz .Lsc_s1
	s_nop 0
	v_mbcnt_lo_u32_b32 v13, vcc_lo, 0
	v_mbcnt_hi_u32_b32 v13, vcc_hi, v13
	v_add_u32_e32 v13, s42, v13
	v_cmp_gt_i32_e64 s[0:1], s7, v13
	s_and_b64 s[4:5], vcc, s[0:1]
	s_and_saveexec_b64 s[0:1], s[4:5]
	v_lshl_add_u32 v14, v13, 4, v9
	v_lshl_add_u32 v15, v13, 2, v10
	v_add_u32_e32 v13, 0x100, v8
	ds_write_b128 v14, v[104:107]
	ds_write_b32 v15, v13
	s_mov_b64 exec, -1
	s_bcnt1_i32_b64 s40, vcc
	s_add_i32 s42, s42, s40
.Lsc_s1:
	s_add_u32 s40, s38, 0x2c00
	buffer_load_dwordx4 v[104:107], v2, s[28:31], s40 offen sc1 nt
	s_waitcnt vmcnt(9)
	v_or3_b32 v12, v108, v109, v110
	v_bitop3_b32 v12, v12, s9, v111 bitop3:0xc8
	v_cmp_ne_u32_e32 vcc, 0, v12
	s_cbranch_vccz .Lsc_s2
	s_nop 0
	v_mbcnt_lo_u32_b32 v13, vcc_lo, 0
	v_mbcnt_hi_u32_b32 v13, vcc_hi, v13
	v_add_u32_e32 v13, s42, v13
	v_cmp_gt_i32_e64 s[0:1], s7, v13
	s_and_b64 s[4:5], vcc, s[0:1]
	s_and_saveexec_b64 s[0:1], s[4:5]
	v_lshl_add_u32 v14, v13, 4, v9
	v_lshl_add_u32 v15, v13, 2, v10
	v_add_u32_e32 v13, 0x200, v8
	ds_write_b128 v14, v[108:111]
	ds_write_b32 v15, v13
	s_mov_b64 exec, -1
	s_bcnt1_i32_b64 s40, vcc
	s_add_i32 s42, s42, s40
.Lsc_s2:
	s_add_u32 s40, s38, 0x3000
	buffer_load_dwordx4 v[108:111], v2, s[28:31], s40 offen sc1 nt
	s_waitcnt vmcnt(9)
	v_or3_b32 v12, v112, v113, v114
	v_bitop3_b32 v12, v12, s9, v115 bitop3:0xc8
	v_cmp_ne_u32_e32 vcc, 0, v12
	s_cbranch_vccz .Lsc_s3
	s_nop 0
	v_mbcnt_lo_u32_b32 v13, vcc_lo, 0
	v_mbcnt_hi_u32_b32 v13, vcc_hi, v13
	v_add_u32_e32 v13, s42, v13
	v_cmp_gt_i32_e64 s[0:1], s7, v13
	s_and_b64 s[4:5], vcc, s[0:1]
	s_and_saveexec_b64 s[0:1], s[4:5]
	v_lshl_add_u32 v14, v13, 4, v9
	v_lshl_add_u32 v15, v13, 2, v10
	v_add_u32_e32 v13, 0x300, v8
	ds_write_b128 v14, v[112:115]
	ds_write_b32 v15, v13
	s_mov_b64 exec, -1
	s_bcnt1_i32_b64 s40, vcc
	s_add_i32 s42, s42, s40
.Lsc_s3:
	s_add_u32 s40, s38, 0x3400
	buffer_load_dwordx4 v[112:115], v2, s[28:31], s40 offen sc1 nt
	s_waitcnt vmcnt(9)
	v_or3_b32 v12, v116, v117, v118
	v_bitop3_b32 v12, v12, s9, v119 bitop3:0xc8
	v_cmp_ne_u32_e32 vcc, 0, v12
	s_cbranch_vccz .Lsc_s4
	s_nop 0
	v_mbcnt_lo_u32_b32 v13, vcc_lo, 0
	v_mbcnt_hi_u32_b32 v13, vcc_hi, v13
	v_add_u32_e32 v13, s42, v13
	v_cmp_gt_i32_e64 s[0:1], s7, v13
	s_and_b64 s[4:5], vcc, s[0:1]
	s_and_saveexec_b64 s[0:1], s[4:5]
	v_lshl_add_u32 v14, v13, 4, v9
	v_lshl_add_u32 v15, v13, 2, v10
	v_add_u32_e32 v13, 0x400, v8
	ds_write_b128 v14, v[116:119]
	ds_write_b32 v15, v13
	s_mov_b64 exec, -1
	s_bcnt1_i32_b64 s40, vcc
	s_add_i32 s42, s42, s40
.Lsc_s4:
	s_add_u32 s40, s38, 0x3800
	buffer_load_dwordx4 v[116:119], v2, s[28:31], s40 offen sc1 nt
	s_waitcnt vmcnt(9)
	v_or3_b32 v12, v120, v121, v122
	v_bitop3_b32 v12, v12, s9, v123 bitop3:0xc8
	v_cmp_ne_u32_e32 vcc, 0, v12
	s_cbranch_vccz .Lsc_s5
	s_nop 0
	v_mbcnt_lo_u32_b32 v13, vcc_lo, 0
	v_mbcnt_hi_u32_b32 v13, vcc_hi, v13
	v_add_u32_e32 v13, s42, v13
	v_cmp_gt_i32_e64 s[0:1], s7, v13
	s_and_b64 s[4:5], vcc, s[0:1]
	s_and_saveexec_b64 s[0:1], s[4:5]
	v_lshl_add_u32 v14, v13, 4, v9
	v_lshl_add_u32 v15, v13, 2, v10
	v_add_u32_e32 v13, 0x500, v8
	ds_write_b128 v14, v[120:123]
	ds_write_b32 v15, v13
	s_mov_b64 exec, -1
	s_bcnt1_i32_b64 s40, vcc
	s_add_i32 s42, s42, s40
.Lsc_s5:
	s_add_u32 s40, s38, 0x3c00
	buffer_load_dwordx4 v[120:123], v2, s[28:31], s40 offen sc1 nt
	s_waitcnt vmcnt(9)
	v_or3_b32 v12, v124, v125, v126
	v_bitop3_b32 v12, v12, s9, v127 bitop3:0xc8
	v_cmp_ne_u32_e32 vcc, 0, v12
	s_cbranch_vccz .Lsc_s6
	s_nop 0
	v_mbcnt_lo_u32_b32 v13, vcc_lo, 0
	v_mbcnt_hi_u32_b32 v13, vcc_hi, v13
	v_add_u32_e32 v13, s42, v13
	v_cmp_gt_i32_e64 s[0:1], s7, v13
	s_and_b64 s[4:5], vcc, s[0:1]
	s_and_saveexec_b64 s[0:1], s[4:5]
	v_lshl_add_u32 v14, v13, 4, v9
	v_lshl_add_u32 v15, v13, 2, v10
	v_add_u32_e32 v13, 0x600, v8
	ds_write_b128 v14, v[124:127]
	ds_write_b32 v15, v13
	s_mov_b64 exec, -1
	s_bcnt1_i32_b64 s40, vcc
	s_add_i32 s42, s42, s40
.Lsc_s6:
	s_add_u32 s40, s38, 0x4000
	buffer_load_dwordx4 v[124:127], v2, s[28:31], s40 offen sc1 nt
	s_waitcnt vmcnt(9)
	v_or3_b32 v12, v128, v129, v130
	v_bitop3_b32 v12, v12, s9, v131 bitop3:0xc8
	v_cmp_ne_u32_e32 vcc, 0, v12
	s_cbranch_vccz .Lsc_s7
	s_nop 0
	v_mbcnt_lo_u32_b32 v13, vcc_lo, 0
	v_mbcnt_hi_u32_b32 v13, vcc_hi, v13
	v_add_u32_e32 v13, s42, v13
	v_cmp_gt_i32_e64 s[0:1], s7, v13
	s_and_b64 s[4:5], vcc, s[0:1]
	s_and_saveexec_b64 s[0:1], s[4:5]
	v_lshl_add_u32 v14, v13, 4, v9
	v_lshl_add_u32 v15, v13, 2, v10
	v_add_u32_e32 v13, 0x700, v8
	ds_write_b128 v14, v[128:131]
	ds_write_b32 v15, v13
	s_mov_b64 exec, -1
	s_bcnt1_i32_b64 s40, vcc
	s_add_i32 s42, s42, s40
.Lsc_s7:
	s_add_u32 s40, s38, 0x4400
	buffer_load_dwordx4 v[128:131], v2, s[28:31], s40 offen sc1 nt
	s_waitcnt vmcnt(9)
	v_or3_b32 v12, v132, v133, v134
	v_bitop3_b32 v12, v12, s9, v135 bitop3:0xc8
	v_cmp_ne_u32_e32 vcc, 0, v12
	s_cbranch_vccz .Lsc_s8
	s_nop 0
	v_mbcnt_lo_u32_b32 v13, vcc_lo, 0
	v_mbcnt_hi_u32_b32 v13, vcc_hi, v13
	v_add_u32_e32 v13, s42, v13
	v_cmp_gt_i32_e64 s[0:1], s7, v13
	s_and_b64 s[4:5], vcc, s[0:1]
	s_and_saveexec_b64 s[0:1], s[4:5]
	v_lshl_add_u32 v14, v13, 4, v9
	v_lshl_add_u32 v15, v13, 2, v10
	v_add_u32_e32 v13, 0x800, v8
	ds_write_b128 v14, v[132:135]
	ds_write_b32 v15, v13
	s_mov_b64 exec, -1
	s_bcnt1_i32_b64 s40, vcc
	s_add_i32 s42, s42, s40
.Lsc_s8:
	s_add_u32 s40, s38, 0x4800
	buffer_load_dwordx4 v[132:135], v2, s[28:31], s40 offen sc1 nt
	s_waitcnt vmcnt(9)
	v_or3_b32 v12, v136, v137, v138
	v_bitop3_b32 v12, v12, s9, v139 bitop3:0xc8
	v_cmp_ne_u32_e32 vcc, 0, v12
	s_cbranch_vccz .Lsc_s9
	s_nop 0
	v_mbcnt_lo_u32_b32 v13, vcc_lo, 0
	v_mbcnt_hi_u32_b32 v13, vcc_hi, v13
	v_add_u32_e32 v13, s42, v13
	v_cmp_gt_i32_e64 s[0:1], s7, v13
	s_and_b64 s[4:5], vcc, s[0:1]
	s_and_saveexec_b64 s[0:1], s[4:5]
	v_lshl_add_u32 v14, v13, 4, v9
	v_lshl_add_u32 v15, v13, 2, v10
	v_add_u32_e32 v13, 0x900, v8
	ds_write_b128 v14, v[136:139]
	ds_write_b32 v15, v13
	s_mov_b64 exec, -1
	s_bcnt1_i32_b64 s40, vcc
	s_add_i32 s42, s42, s40
.Lsc_s9:
	s_add_u32 s40, s38, 0x4c00
	buffer_load_dwordx4 v[136:139], v2, s[28:31], s40 offen sc1 nt
	s_waitcnt vmcnt(9)
	v_or3_b32 v12, v100, v101, v102
	v_bitop3_b32 v12, v12, s9, v103 bitop3:0xc8
	v_cmp_ne_u32_e32 vcc, 0, v12
	s_cbranch_vccz .Lsc_s10
	s_nop 0
	v_mbcnt_lo_u32_b32 v13, vcc_lo, 0
	v_mbcnt_hi_u32_b32 v13, vcc_hi, v13
	v_add_u32_e32 v13, s42, v13
	v_cmp_gt_i32_e64 s[0:1], s7, v13
	s_and_b64 s[4:5], vcc, s[0:1]
	s_and_saveexec_b64 s[0:1], s[4:5]
	v_lshl_add_u32 v14, v13, 4, v9
	v_lshl_add_u32 v15, v13, 2, v10
	v_add_u32_e32 v13, 0xa00, v8
	ds_write_b128 v14, v[100:103]
	ds_write_b32 v15, v13
	s_mov_b64 exec, -1
	s_bcnt1_i32_b64 s40, vcc
	s_add_i32 s42, s42, s40
.Lsc_s10:
	s_add_u32 s40, s38, 0x5000
	buffer_load_dwordx4 v[100:103], v2, s[28:31], s40 offen sc1 nt
	s_waitcnt vmcnt(9)
	v_or3_b32 v12, v104, v105, v106
	v_bitop3_b32 v12, v12, s9, v107 bitop3:0xc8
	v_cmp_ne_u32_e32 vcc, 0, v12
	s_cbranch_vccz .Lsc_s11
	s_nop 0
	v_mbcnt_lo_u32_b32 v13, vcc_lo, 0
	v_mbcnt_hi_u32_b32 v13, vcc_hi, v13
	v_add_u32_e32 v13, s42, v13
	v_cmp_gt_i32_e64 s[0:1], s7, v13
	s_and_b64 s[4:5], vcc, s[0:1]
	s_and_saveexec_b64 s[0:1], s[4:5]
	v_lshl_add_u32 v14, v13, 4, v9
	v_lshl_add_u32 v15, v13, 2, v10
	v_add_u32_e32 v13, 0xb00, v8
	ds_write_b128 v14, v[104:107]
	ds_write_b32 v15, v13
	s_mov_b64 exec, -1
	s_bcnt1_i32_b64 s40, vcc
	s_add_i32 s42, s42, s40
.Lsc_s11:
	s_add_u32 s40, s38, 0x5400
	buffer_load_dwordx4 v[104:107], v2, s[28:31], s40 offen sc1 nt
	s_waitcnt vmcnt(9)
	v_or3_b32 v12, v108, v109, v110
	v_bitop3_b32 v12, v12, s9, v111 bitop3:0xc8
	v_cmp_ne_u32_e32 vcc, 0, v12
	s_cbranch_vccz .Lsc_s12
	s_nop 0
	v_mbcnt_lo_u32_b32 v13, vcc_lo, 0
	v_mbcnt_hi_u32_b32 v13, vcc_hi, v13
	v_add_u32_e32 v13, s42, v13
	v_cmp_gt_i32_e64 s[0:1], s7, v13
	s_and_b64 s[4:5], vcc, s[0:1]
	s_and_saveexec_b64 s[0:1], s[4:5]
	v_lshl_add_u32 v14, v13, 4, v9
	v_lshl_add_u32 v15, v13, 2, v10
	v_add_u32_e32 v13, 0xc00, v8
	ds_write_b128 v14, v[108:111]
	ds_write_b32 v15, v13
	s_mov_b64 exec, -1
	s_bcnt1_i32_b64 s40, vcc
	s_add_i32 s42, s42, s40
.Lsc_s12:
	s_add_u32 s40, s38, 0x5800
	buffer_load_dwordx4 v[108:111], v2, s[28:31], s40 offen sc1 nt
	s_waitcnt vmcnt(9)
	v_or3_b32 v12, v112, v113, v114
	v_bitop3_b32 v12, v12, s9, v115 bitop3:0xc8
	v_cmp_ne_u32_e32 vcc, 0, v12
	s_cbranch_vccz .Lsc_s13
	s_nop 0
	v_mbcnt_lo_u32_b32 v13, vcc_lo, 0
	v_mbcnt_hi_u32_b32 v13, vcc_hi, v13
	v_add_u32_e32 v13, s42, v13
	v_cmp_gt_i32_e64 s[0:1], s7, v13
	s_and_b64 s[4:5], vcc, s[0:1]
	s_and_saveexec_b64 s[0:1], s[4:5]
	v_lshl_add_u32 v14, v13, 4, v9
	v_lshl_add_u32 v15, v13, 2, v10
	v_add_u32_e32 v13, 0xd00, v8
	ds_write_b128 v14, v[112:115]
	ds_write_b32 v15, v13
	s_mov_b64 exec, -1
	s_bcnt1_i32_b64 s40, vcc
	s_add_i32 s42, s42, s40
.Lsc_s13:
	s_add_u32 s40, s38, 0x5c00
	buffer_load_dwordx4 v[112:115], v2, s[28:31], s40 offen sc1 nt
	s_waitcnt vmcnt(9)
	v_or3_b32 v12, v116, v117, v118
	v_bitop3_b32 v12, v12, s9, v119 bitop3:0xc8
	v_cmp_ne_u32_e32 vcc, 0, v12
	s_cbranch_vccz .Lsc_s14
	s_nop 0
	v_mbcnt_lo_u32_b32 v13, vcc_lo, 0
	v_mbcnt_hi_u32_b32 v13, vcc_hi, v13
	v_add_u32_e32 v13, s42, v13
	v_cmp_gt_i32_e64 s[0:1], s7, v13
	s_and_b64 s[4:5], vcc, s[0:1]
	s_and_saveexec_b64 s[0:1], s[4:5]
	v_lshl_add_u32 v14, v13, 4, v9
	v_lshl_add_u32 v15, v13, 2, v10
	v_add_u32_e32 v13, 0xe00, v8
	ds_write_b128 v14, v[116:119]
	ds_write_b32 v15, v13
	s_mov_b64 exec, -1
	s_bcnt1_i32_b64 s40, vcc
	s_add_i32 s42, s42, s40
.Lsc_s14:
	s_add_u32 s40, s38, 0x6000
	buffer_load_dwordx4 v[116:119], v2, s[28:31], s40 offen sc1 nt
	s_waitcnt vmcnt(9)
	v_or3_b32 v12, v120, v121, v122
	v_bitop3_b32 v12, v12, s9, v123 bitop3:0xc8
	v_cmp_ne_u32_e32 vcc, 0, v12
	s_cbranch_vccz .Lsc_s15
	s_nop 0
	v_mbcnt_lo_u32_b32 v13, vcc_lo, 0
	v_mbcnt_hi_u32_b32 v13, vcc_hi, v13
	v_add_u32_e32 v13, s42, v13
	v_cmp_gt_i32_e64 s[0:1], s7, v13
	s_and_b64 s[4:5], vcc, s[0:1]
	s_and_saveexec_b64 s[0:1], s[4:5]
	v_lshl_add_u32 v14, v13, 4, v9
	v_lshl_add_u32 v15, v13, 2, v10
	v_add_u32_e32 v13, 0xf00, v8
	ds_write_b128 v14, v[120:123]
	ds_write_b32 v15, v13
	s_mov_b64 exec, -1
	s_bcnt1_i32_b64 s40, vcc
	s_add_i32 s42, s42, s40
.Lsc_s15:
	s_add_u32 s40, s38, 0x6400
	buffer_load_dwordx4 v[120:123], v2, s[28:31], s40 offen sc1 nt
	s_waitcnt vmcnt(9)
	v_or3_b32 v12, v124, v125, v126
	v_bitop3_b32 v12, v12, s9, v127 bitop3:0xc8
	v_cmp_ne_u32_e32 vcc, 0, v12
	s_cbranch_vccz .Lsc_s16
	s_nop 0
	v_mbcnt_lo_u32_b32 v13, vcc_lo, 0
	v_mbcnt_hi_u32_b32 v13, vcc_hi, v13
	v_add_u32_e32 v13, s42, v13
	v_cmp_gt_i32_e64 s[0:1], s7, v13
	s_and_b64 s[4:5], vcc, s[0:1]
	s_and_saveexec_b64 s[0:1], s[4:5]
	v_lshl_add_u32 v14, v13, 4, v9
	v_lshl_add_u32 v15, v13, 2, v10
	v_add_u32_e32 v13, 0x1000, v8
	ds_write_b128 v14, v[124:127]
	ds_write_b32 v15, v13
	s_mov_b64 exec, -1
	s_bcnt1_i32_b64 s40, vcc
	s_add_i32 s42, s42, s40
.Lsc_s16:
	s_add_u32 s40, s38, 0x6800
	buffer_load_dwordx4 v[124:127], v2, s[28:31], s40 offen sc1 nt
	s_waitcnt vmcnt(9)
	v_or3_b32 v12, v128, v129, v130
	v_bitop3_b32 v12, v12, s9, v131 bitop3:0xc8
	v_cmp_ne_u32_e32 vcc, 0, v12
	s_cbranch_vccz .Lsc_s17
	s_nop 0
	v_mbcnt_lo_u32_b32 v13, vcc_lo, 0
	v_mbcnt_hi_u32_b32 v13, vcc_hi, v13
	v_add_u32_e32 v13, s42, v13
	v_cmp_gt_i32_e64 s[0:1], s7, v13
	s_and_b64 s[4:5], vcc, s[0:1]
	s_and_saveexec_b64 s[0:1], s[4:5]
	v_lshl_add_u32 v14, v13, 4, v9
	v_lshl_add_u32 v15, v13, 2, v10
	v_add_u32_e32 v13, 0x1100, v8
	ds_write_b128 v14, v[128:131]
	ds_write_b32 v15, v13
	s_mov_b64 exec, -1
	s_bcnt1_i32_b64 s40, vcc
	s_add_i32 s42, s42, s40
.Lsc_s17:
	s_add_u32 s40, s38, 0x6c00
	buffer_load_dwordx4 v[128:131], v2, s[28:31], s40 offen sc1 nt
	s_waitcnt vmcnt(9)
	v_or3_b32 v12, v132, v133, v134
	v_bitop3_b32 v12, v12, s9, v135 bitop3:0xc8
	v_cmp_ne_u32_e32 vcc, 0, v12
	s_cbranch_vccz .Lsc_s18
	s_nop 0
	v_mbcnt_lo_u32_b32 v13, vcc_lo, 0
	v_mbcnt_hi_u32_b32 v13, vcc_hi, v13
	v_add_u32_e32 v13, s42, v13
	v_cmp_gt_i32_e64 s[0:1], s7, v13
	s_and_b64 s[4:5], vcc, s[0:1]
	s_and_saveexec_b64 s[0:1], s[4:5]
	v_lshl_add_u32 v14, v13, 4, v9
	v_lshl_add_u32 v15, v13, 2, v10
	v_add_u32_e32 v13, 0x1200, v8
	ds_write_b128 v14, v[132:135]
	ds_write_b32 v15, v13
	s_mov_b64 exec, -1
	s_bcnt1_i32_b64 s40, vcc
	s_add_i32 s42, s42, s40
.Lsc_s18:
	s_add_u32 s40, s38, 0x7000
	buffer_load_dwordx4 v[132:135], v2, s[28:31], s40 offen sc1 nt
	s_waitcnt vmcnt(9)
	v_or3_b32 v12, v136, v137, v138
	v_bitop3_b32 v12, v12, s9, v139 bitop3:0xc8
	v_cmp_ne_u32_e32 vcc, 0, v12
	s_cbranch_vccz .Lsc_s19
	s_nop 0
	v_mbcnt_lo_u32_b32 v13, vcc_lo, 0
	v_mbcnt_hi_u32_b32 v13, vcc_hi, v13
	v_add_u32_e32 v13, s42, v13
	v_cmp_gt_i32_e64 s[0:1], s7, v13
	s_and_b64 s[4:5], vcc, s[0:1]
	s_and_saveexec_b64 s[0:1], s[4:5]
	v_lshl_add_u32 v14, v13, 4, v9
	v_lshl_add_u32 v15, v13, 2, v10
	v_add_u32_e32 v13, 0x1300, v8
	ds_write_b128 v14, v[136:139]
	ds_write_b32 v15, v13
	s_mov_b64 exec, -1
	s_bcnt1_i32_b64 s40, vcc
	s_add_i32 s42, s42, s40
.Lsc_s19:
	s_add_u32 s40, s38, 0x7400
	buffer_load_dwordx4 v[136:139], v2, s[28:31], s40 offen sc1 nt
	s_waitcnt vmcnt(9)
	v_or3_b32 v12, v100, v101, v102
	v_bitop3_b32 v12, v12, s9, v103 bitop3:0xc8
	v_cmp_ne_u32_e32 vcc, 0, v12
	s_cbranch_vccz .Lsc_s20
	s_nop 0
	v_mbcnt_lo_u32_b32 v13, vcc_lo, 0
	v_mbcnt_hi_u32_b32 v13, vcc_hi, v13
	v_add_u32_e32 v13, s42, v13
	v_cmp_gt_i32_e64 s[0:1], s7, v13
	s_and_b64 s[4:5], vcc, s[0:1]
	s_and_saveexec_b64 s[0:1], s[4:5]
	v_lshl_add_u32 v14, v13, 4, v9
	v_lshl_add_u32 v15, v13, 2, v10
	v_add_u32_e32 v13, 0x1400, v8
	ds_write_b128 v14, v[100:103]
	ds_write_b32 v15, v13
	s_mov_b64 exec, -1
	s_bcnt1_i32_b64 s40, vcc
	s_add_i32 s42, s42, s40
.Lsc_s20:
	s_add_u32 s40, s38, 0x7800
	buffer_load_dwordx4 v[100:103], v2, s[28:31], s40 offen sc1 nt
	s_waitcnt vmcnt(9)
	v_or3_b32 v12, v104, v105, v106
	v_bitop3_b32 v12, v12, s9, v107 bitop3:0xc8
	v_cmp_ne_u32_e32 vcc, 0, v12
	s_cbranch_vccz .Lsc_s21
	s_nop 0
	v_mbcnt_lo_u32_b32 v13, vcc_lo, 0
	v_mbcnt_hi_u32_b32 v13, vcc_hi, v13
	v_add_u32_e32 v13, s42, v13
	v_cmp_gt_i32_e64 s[0:1], s7, v13
	s_and_b64 s[4:5], vcc, s[0:1]
	s_and_saveexec_b64 s[0:1], s[4:5]
	v_lshl_add_u32 v14, v13, 4, v9
	v_lshl_add_u32 v15, v13, 2, v10
	v_add_u32_e32 v13, 0x1500, v8
	ds_write_b128 v14, v[104:107]
	ds_write_b32 v15, v13
	s_mov_b64 exec, -1
	s_bcnt1_i32_b64 s40, vcc
	s_add_i32 s42, s42, s40
.Lsc_s21:
	s_add_u32 s40, s38, 0x7c00
	buffer_load_dwordx4 v[104:107], v2, s[28:31], s40 offen sc1 nt
	s_waitcnt vmcnt(9)
	v_or3_b32 v12, v108, v109, v110
	v_bitop3_b32 v12, v12, s9, v111 bitop3:0xc8
	v_cmp_ne_u32_e32 vcc, 0, v12
	s_cbranch_vccz .Lsc_s22
	s_nop 0
	v_mbcnt_lo_u32_b32 v13, vcc_lo, 0
	v_mbcnt_hi_u32_b32 v13, vcc_hi, v13
	v_add_u32_e32 v13, s42, v13
	v_cmp_gt_i32_e64 s[0:1], s7, v13
	s_and_b64 s[4:5], vcc, s[0:1]
	s_and_saveexec_b64 s[0:1], s[4:5]
	v_lshl_add_u32 v14, v13, 4, v9
	v_lshl_add_u32 v15, v13, 2, v10
	v_add_u32_e32 v13, 0x1600, v8
	ds_write_b128 v14, v[108:111]
	ds_write_b32 v15, v13
	s_mov_b64 exec, -1
	s_bcnt1_i32_b64 s40, vcc
	s_add_i32 s42, s42, s40
.Lsc_s22:
	s_add_u32 s40, s38, 0x8000
	buffer_load_dwordx4 v[108:111], v2, s[28:31], s40 offen sc1 nt
	s_waitcnt vmcnt(9)
	v_or3_b32 v12, v112, v113, v114
	v_bitop3_b32 v12, v12, s9, v115 bitop3:0xc8
	v_cmp_ne_u32_e32 vcc, 0, v12
	s_cbranch_vccz .Lsc_s23
	s_nop 0
	v_mbcnt_lo_u32_b32 v13, vcc_lo, 0
	v_mbcnt_hi_u32_b32 v13, vcc_hi, v13
	v_add_u32_e32 v13, s42, v13
	v_cmp_gt_i32_e64 s[0:1], s7, v13
	s_and_b64 s[4:5], vcc, s[0:1]
	s_and_saveexec_b64 s[0:1], s[4:5]
	v_lshl_add_u32 v14, v13, 4, v9
	v_lshl_add_u32 v15, v13, 2, v10
	v_add_u32_e32 v13, 0x1700, v8
	ds_write_b128 v14, v[112:115]
	ds_write_b32 v15, v13
	s_mov_b64 exec, -1
	s_bcnt1_i32_b64 s40, vcc
	s_add_i32 s42, s42, s40
.Lsc_s23:
	s_add_u32 s40, s38, 0x8400
	buffer_load_dwordx4 v[112:115], v2, s[28:31], s40 offen sc1 nt
	s_waitcnt vmcnt(9)
	v_or3_b32 v12, v116, v117, v118
	v_bitop3_b32 v12, v12, s9, v119 bitop3:0xc8
	v_cmp_ne_u32_e32 vcc, 0, v12
	s_cbranch_vccz .Lsc_s24
	s_nop 0
	v_mbcnt_lo_u32_b32 v13, vcc_lo, 0
	v_mbcnt_hi_u32_b32 v13, vcc_hi, v13
	v_add_u32_e32 v13, s42, v13
	v_cmp_gt_i32_e64 s[0:1], s7, v13
	s_and_b64 s[4:5], vcc, s[0:1]
	s_and_saveexec_b64 s[0:1], s[4:5]
	v_lshl_add_u32 v14, v13, 4, v9
	v_lshl_add_u32 v15, v13, 2, v10
	v_add_u32_e32 v13, 0x1800, v8
	ds_write_b128 v14, v[116:119]
	ds_write_b32 v15, v13
	s_mov_b64 exec, -1
	s_bcnt1_i32_b64 s40, vcc
	s_add_i32 s42, s42, s40
.Lsc_s24:
	s_add_u32 s40, s38, 0x8800
	buffer_load_dwordx4 v[116:119], v2, s[28:31], s40 offen sc1 nt
	s_waitcnt vmcnt(9)
	v_or3_b32 v12, v120, v121, v122
	v_bitop3_b32 v12, v12, s9, v123 bitop3:0xc8
	v_cmp_ne_u32_e32 vcc, 0, v12
	s_cbranch_vccz .Lsc_s25
	s_nop 0
	v_mbcnt_lo_u32_b32 v13, vcc_lo, 0
	v_mbcnt_hi_u32_b32 v13, vcc_hi, v13
	v_add_u32_e32 v13, s42, v13
	v_cmp_gt_i32_e64 s[0:1], s7, v13
	s_and_b64 s[4:5], vcc, s[0:1]
	s_and_saveexec_b64 s[0:1], s[4:5]
	v_lshl_add_u32 v14, v13, 4, v9
	v_lshl_add_u32 v15, v13, 2, v10
	v_add_u32_e32 v13, 0x1900, v8
	ds_write_b128 v14, v[120:123]
	ds_write_b32 v15, v13
	s_mov_b64 exec, -1
	s_bcnt1_i32_b64 s40, vcc
	s_add_i32 s42, s42, s40
.Lsc_s25:
	s_add_u32 s40, s38, 0x8c00
	buffer_load_dwordx4 v[120:123], v2, s[28:31], s40 offen sc1 nt
	s_waitcnt vmcnt(9)
	v_or3_b32 v12, v124, v125, v126
	v_bitop3_b32 v12, v12, s9, v127 bitop3:0xc8
	v_cmp_ne_u32_e32 vcc, 0, v12
	s_cbranch_vccz .Lsc_s26
	s_nop 0
	v_mbcnt_lo_u32_b32 v13, vcc_lo, 0
	v_mbcnt_hi_u32_b32 v13, vcc_hi, v13
	v_add_u32_e32 v13, s42, v13
	v_cmp_gt_i32_e64 s[0:1], s7, v13
	s_and_b64 s[4:5], vcc, s[0:1]
	s_and_saveexec_b64 s[0:1], s[4:5]
	v_lshl_add_u32 v14, v13, 4, v9
	v_lshl_add_u32 v15, v13, 2, v10
	v_add_u32_e32 v13, 0x1a00, v8
	ds_write_b128 v14, v[124:127]
	ds_write_b32 v15, v13
	s_mov_b64 exec, -1
	s_bcnt1_i32_b64 s40, vcc
	s_add_i32 s42, s42, s40
.Lsc_s26:
	s_add_u32 s40, s38, 0x9000
	buffer_load_dwordx4 v[124:127], v2, s[28:31], s40 offen sc1 nt
	s_waitcnt vmcnt(9)
	v_or3_b32 v12, v128, v129, v130
	v_bitop3_b32 v12, v12, s9, v131 bitop3:0xc8
	v_cmp_ne_u32_e32 vcc, 0, v12
	s_cbranch_vccz .Lsc_s27
	s_nop 0
	v_mbcnt_lo_u32_b32 v13, vcc_lo, 0
	v_mbcnt_hi_u32_b32 v13, vcc_hi, v13
	v_add_u32_e32 v13, s42, v13
	v_cmp_gt_i32_e64 s[0:1], s7, v13
	s_and_b64 s[4:5], vcc, s[0:1]
	s_and_saveexec_b64 s[0:1], s[4:5]
	v_lshl_add_u32 v14, v13, 4, v9
	v_lshl_add_u32 v15, v13, 2, v10
	v_add_u32_e32 v13, 0x1b00, v8
	ds_write_b128 v14, v[128:131]
	ds_write_b32 v15, v13
	s_mov_b64 exec, -1
	s_bcnt1_i32_b64 s40, vcc
	s_add_i32 s42, s42, s40
.Lsc_s27:
	s_add_u32 s40, s38, 0x9400
	buffer_load_dwordx4 v[128:131], v2, s[28:31], s40 offen sc1 nt
	s_waitcnt vmcnt(9)
	v_or3_b32 v12, v132, v133, v134
	v_bitop3_b32 v12, v12, s9, v135 bitop3:0xc8
	v_cmp_ne_u32_e32 vcc, 0, v12
	s_cbranch_vccz .Lsc_s28
	s_nop 0
	v_mbcnt_lo_u32_b32 v13, vcc_lo, 0
	v_mbcnt_hi_u32_b32 v13, vcc_hi, v13
	v_add_u32_e32 v13, s42, v13
	v_cmp_gt_i32_e64 s[0:1], s7, v13
	s_and_b64 s[4:5], vcc, s[0:1]
	s_and_saveexec_b64 s[0:1], s[4:5]
	v_lshl_add_u32 v14, v13, 4, v9
	v_lshl_add_u32 v15, v13, 2, v10
	v_add_u32_e32 v13, 0x1c00, v8
	ds_write_b128 v14, v[132:135]
	ds_write_b32 v15, v13
	s_mov_b64 exec, -1
	s_bcnt1_i32_b64 s40, vcc
	s_add_i32 s42, s42, s40
.Lsc_s28:
	s_add_u32 s40, s38, 0x9800
	buffer_load_dwordx4 v[132:135], v2, s[28:31], s40 offen sc1 nt
	s_waitcnt vmcnt(9)
	v_or3_b32 v12, v136, v137, v138
	v_bitop3_b32 v12, v12, s9, v139 bitop3:0xc8
	v_cmp_ne_u32_e32 vcc, 0, v12
	s_cbranch_vccz .Lsc_s29
	s_nop 0
	v_mbcnt_lo_u32_b32 v13, vcc_lo, 0
	v_mbcnt_hi_u32_b32 v13, vcc_hi, v13
	v_add_u32_e32 v13, s42, v13
	v_cmp_gt_i32_e64 s[0:1], s7, v13
	s_and_b64 s[4:5], vcc, s[0:1]
	s_and_saveexec_b64 s[0:1], s[4:5]
	v_lshl_add_u32 v14, v13, 4, v9
	v_lshl_add_u32 v15, v13, 2, v10
	v_add_u32_e32 v13, 0x1d00, v8
	ds_write_b128 v14, v[136:139]
	ds_write_b32 v15, v13
	s_mov_b64 exec, -1
	s_bcnt1_i32_b64 s40, vcc
	s_add_i32 s42, s42, s40
.Lsc_s29:
	s_add_u32 s40, s38, 0x9c00
	buffer_load_dwordx4 v[136:139], v4, s[28:31], s40 offen sc1 nt
	s_waitcnt vmcnt(9)
	v_or3_b32 v12, v100, v101, v102
	v_bitop3_b32 v12, v12, s9, v103 bitop3:0xc8
	v_cmp_ne_u32_e32 vcc, 0, v12
	s_cbranch_vccz .Lsc_s30
	s_nop 0
	v_mbcnt_lo_u32_b32 v13, vcc_lo, 0
	v_mbcnt_hi_u32_b32 v13, vcc_hi, v13
	v_add_u32_e32 v13, s42, v13
	v_cmp_gt_i32_e64 s[0:1], s7, v13
	s_and_b64 s[4:5], vcc, s[0:1]
	s_and_saveexec_b64 s[0:1], s[4:5]
	v_lshl_add_u32 v14, v13, 4, v9
	v_lshl_add_u32 v15, v13, 2, v10
	v_add_u32_e32 v13, 0x1e00, v8
	ds_write_b128 v14, v[100:103]
	ds_write_b32 v15, v13
	s_mov_b64 exec, -1
	s_bcnt1_i32_b64 s40, vcc
	s_add_i32 s42, s42, s40
.Lsc_s30:
	s_mov_b32 s40, s39
	buffer_load_dwordx4 v[100:103], v5, s[28:31], s40 offen sc1 nt
	s_waitcnt vmcnt(9)
	v_or3_b32 v12, v104, v105, v106
	v_bitop3_b32 v12, v12, s9, v107 bitop3:0xc8
	v_cmp_ne_u32_e32 vcc, 0, v12
	s_cbranch_vccz .Lsc_s31
	s_nop 0
	v_mbcnt_lo_u32_b32 v13, vcc_lo, 0
	v_mbcnt_hi_u32_b32 v13, vcc_hi, v13
	v_add_u32_e32 v13, s42, v13
	v_cmp_gt_i32_e64 s[0:1], s7, v13
	s_and_b64 s[4:5], vcc, s[0:1]
	s_and_saveexec_b64 s[0:1], s[4:5]
	v_lshl_add_u32 v14, v13, 4, v9
	v_lshl_add_u32 v15, v13, 2, v10
	v_add_u32_e32 v13, 0x1f00, v8
	ds_write_b128 v14, v[104:107]
	ds_write_b32 v15, v13
	s_mov_b64 exec, -1
	s_bcnt1_i32_b64 s40, vcc
	s_add_i32 s42, s42, s40
.Lsc_s31:
	s_add_u32 s40, s39, 0x400
	buffer_load_dwordx4 v[104:107], v6, s[28:31], s40 offen sc1 nt
	s_waitcnt vmcnt(9)
	v_or3_b32 v12, v108, v109, v110
	v_bitop3_b32 v12, v12, s9, v111 bitop3:0xc8
	v_cmp_ne_u32_e32 vcc, 0, v12
	s_cbranch_vccz .Lsc_s32
	s_nop 0
	v_mbcnt_lo_u32_b32 v13, vcc_lo, 0
	v_mbcnt_hi_u32_b32 v13, vcc_hi, v13
	v_add_u32_e32 v13, s42, v13
	v_cmp_gt_i32_e64 s[0:1], s7, v13
	s_and_b64 s[4:5], vcc, s[0:1]
	s_and_saveexec_b64 s[0:1], s[4:5]
	v_lshl_add_u32 v14, v13, 4, v9
	v_lshl_add_u32 v15, v13, 2, v10
	v_add_u32_e32 v13, 0x2000, v8
	ds_write_b128 v14, v[108:111]
	ds_write_b32 v15, v13
	s_mov_b64 exec, -1
	s_bcnt1_i32_b64 s40, vcc
	s_add_i32 s42, s42, s40
.Lsc_s32:
	s_add_u32 s40, s39, 0x800
	buffer_load_dwordx4 v[108:111], v6, s[28:31], s40 offen sc1 nt
	s_waitcnt vmcnt(9)
	v_or3_b32 v12, v112, v113, v114
	v_bitop3_b32 v12, v12, s9, v115 bitop3:0xc8
	v_cmp_ne_u32_e32 vcc, 0, v12
	s_cbranch_vccz .Lsc_s33
	s_nop 0
	v_mbcnt_lo_u32_b32 v13, vcc_lo, 0
	v_mbcnt_hi_u32_b32 v13, vcc_hi, v13
	v_add_u32_e32 v13, s42, v13
	v_cmp_gt_i32_e64 s[0:1], s7, v13
	s_and_b64 s[4:5], vcc, s[0:1]
	s_and_saveexec_b64 s[0:1], s[4:5]
	v_lshl_add_u32 v14, v13, 4, v9
	v_lshl_add_u32 v15, v13, 2, v10
	v_add_u32_e32 v13, 0x2100, v8
	ds_write_b128 v14, v[112:115]
	ds_write_b32 v15, v13
	s_mov_b64 exec, -1
	s_bcnt1_i32_b64 s40, vcc
	s_add_i32 s42, s42, s40
.Lsc_s33:
	s_add_u32 s40, s39, 0xc00
	buffer_load_dwordx4 v[112:115], v6, s[28:31], s40 offen sc1 nt
	s_waitcnt vmcnt(9)
	v_or3_b32 v12, v116, v117, v118
	v_bitop3_b32 v12, v12, s9, v119 bitop3:0xc8
	v_cmp_ne_u32_e32 vcc, 0, v12
	s_cbranch_vccz .Lsc_s34
	s_nop 0
	v_mbcnt_lo_u32_b32 v13, vcc_lo, 0
	v_mbcnt_hi_u32_b32 v13, vcc_hi, v13
	v_add_u32_e32 v13, s42, v13
	v_cmp_gt_i32_e64 s[0:1], s7, v13
	s_and_b64 s[4:5], vcc, s[0:1]
	s_and_saveexec_b64 s[0:1], s[4:5]
	v_lshl_add_u32 v14, v13, 4, v9
	v_lshl_add_u32 v15, v13, 2, v10
	v_add_u32_e32 v13, 0x2200, v8
	ds_write_b128 v14, v[116:119]
	ds_write_b32 v15, v13
	s_mov_b64 exec, -1
	s_bcnt1_i32_b64 s40, vcc
	s_add_i32 s42, s42, s40
.Lsc_s34:
	s_add_u32 s40, s39, 0x1000
	buffer_load_dwordx4 v[116:119], v6, s[28:31], s40 offen sc1 nt
	s_waitcnt vmcnt(9)
	v_or3_b32 v12, v120, v121, v122
	v_bitop3_b32 v12, v12, s9, v123 bitop3:0xc8
	v_cmp_ne_u32_e32 vcc, 0, v12
	s_cbranch_vccz .Lsc_s35
	s_nop 0
	v_mbcnt_lo_u32_b32 v13, vcc_lo, 0
	v_mbcnt_hi_u32_b32 v13, vcc_hi, v13
	v_add_u32_e32 v13, s42, v13
	v_cmp_gt_i32_e64 s[0:1], s7, v13
	s_and_b64 s[4:5], vcc, s[0:1]
	s_and_saveexec_b64 s[0:1], s[4:5]
	v_lshl_add_u32 v14, v13, 4, v9
	v_lshl_add_u32 v15, v13, 2, v10
	v_add_u32_e32 v13, 0x2300, v8
	ds_write_b128 v14, v[120:123]
	ds_write_b32 v15, v13
	s_mov_b64 exec, -1
	s_bcnt1_i32_b64 s40, vcc
	s_add_i32 s42, s42, s40
.Lsc_s35:
	s_add_u32 s40, s39, 0x1400
	buffer_load_dwordx4 v[120:123], v6, s[28:31], s40 offen sc1 nt
	s_waitcnt vmcnt(9)
	v_or3_b32 v12, v124, v125, v126
	v_bitop3_b32 v12, v12, s9, v127 bitop3:0xc8
	v_cmp_ne_u32_e32 vcc, 0, v12
	s_cbranch_vccz .Lsc_s36
	s_nop 0
	v_mbcnt_lo_u32_b32 v13, vcc_lo, 0
	v_mbcnt_hi_u32_b32 v13, vcc_hi, v13
	v_add_u32_e32 v13, s42, v13
	v_cmp_gt_i32_e64 s[0:1], s7, v13
	s_and_b64 s[4:5], vcc, s[0:1]
	s_and_saveexec_b64 s[0:1], s[4:5]
	v_lshl_add_u32 v14, v13, 4, v9
	v_lshl_add_u32 v15, v13, 2, v10
	v_add_u32_e32 v13, 0x2400, v8
	ds_write_b128 v14, v[124:127]
	ds_write_b32 v15, v13
	s_mov_b64 exec, -1
	s_bcnt1_i32_b64 s40, vcc
	s_add_i32 s42, s42, s40
.Lsc_s36:
	s_add_u32 s40, s39, 0x1800
	buffer_load_dwordx4 v[124:127], v6, s[28:31], s40 offen sc1 nt
	s_waitcnt vmcnt(9)
	v_or3_b32 v12, v128, v129, v130
	v_bitop3_b32 v12, v12, s9, v131 bitop3:0xc8
	v_cmp_ne_u32_e32 vcc, 0, v12
	s_cbranch_vccz .Lsc_s37
	s_nop 0
	v_mbcnt_lo_u32_b32 v13, vcc_lo, 0
	v_mbcnt_hi_u32_b32 v13, vcc_hi, v13
	v_add_u32_e32 v13, s42, v13
	v_cmp_gt_i32_e64 s[0:1], s7, v13
	s_and_b64 s[4:5], vcc, s[0:1]
	s_and_saveexec_b64 s[0:1], s[4:5]
	v_lshl_add_u32 v14, v13, 4, v9
	v_lshl_add_u32 v15, v13, 2, v10
	v_add_u32_e32 v13, 0x2500, v8
	ds_write_b128 v14, v[128:131]
	ds_write_b32 v15, v13
	s_mov_b64 exec, -1
	s_bcnt1_i32_b64 s40, vcc
	s_add_i32 s42, s42, s40
.Lsc_s37:
	s_add_u32 s40, s39, 0x1c00
	buffer_load_dwordx4 v[128:131], v6, s[28:31], s40 offen sc1 nt
	s_waitcnt vmcnt(9)
	v_or3_b32 v12, v132, v133, v134
	v_bitop3_b32 v12, v12, s9, v135 bitop3:0xc8
	v_cmp_ne_u32_e32 vcc, 0, v12
	s_cbranch_vccz .Lsc_s38
	s_nop 0
	v_mbcnt_lo_u32_b32 v13, vcc_lo, 0
	v_mbcnt_hi_u32_b32 v13, vcc_hi, v13
	v_add_u32_e32 v13, s42, v13
	v_cmp_gt_i32_e64 s[0:1], s7, v13
	s_and_b64 s[4:5], vcc, s[0:1]
	s_and_saveexec_b64 s[0:1], s[4:5]
	v_lshl_add_u32 v14, v13, 4, v9
	v_lshl_add_u32 v15, v13, 2, v10
	v_add_u32_e32 v13, 0x2600, v8
	ds_write_b128 v14, v[132:135]
	ds_write_b32 v15, v13
	s_mov_b64 exec, -1
	s_bcnt1_i32_b64 s40, vcc
	s_add_i32 s42, s42, s40
.Lsc_s38:
	s_add_u32 s40, s39, 0x2000
	buffer_load_dwordx4 v[132:135], v6, s[28:31], s40 offen sc1 nt
	s_waitcnt vmcnt(9)
	v_or3_b32 v12, v136, v137, v138
	v_bitop3_b32 v12, v12, s9, v139 bitop3:0xc8
	v_cmp_ne_u32_e32 vcc, 0, v12
	s_and_b64 vcc, vcc, s[50:51]
	s_cbranch_vccz .Lsc_s39
	s_nop 0
	v_mbcnt_lo_u32_b32 v13, vcc_lo, 0
	v_mbcnt_hi_u32_b32 v13, vcc_hi, v13
	v_add_u32_e32 v13, s42, v13
	v_cmp_gt_i32_e64 s[0:1], s7, v13
	s_and_b64 s[4:5], vcc, s[0:1]
	s_and_saveexec_b64 s[0:1], s[4:5]
	v_lshl_add_u32 v14, v13, 4, v9
	v_lshl_add_u32 v15, v13, 2, v10
	v_add_u32_e32 v13, 0x2700, v8
	ds_write_b128 v14, v[136:139]
	ds_write_b32 v15, v13
	s_mov_b64 exec, -1
	s_bcnt1_i32_b64 s40, vcc
	s_add_i32 s42, s42, s40
.Lsc_s39:
	s_add_u32 s40, s39, 0x2400
	buffer_load_dwordx4 v[136:139], v6, s[28:31], s40 offen sc1 nt
	s_waitcnt lgkmcnt(0)
	s_add_i32 s42, s42, 1
	v_mov_b32_e32 v12, s42
	ds_write_b32 v11, v12
	s_cmp_eq_u32 s35, s36
	s_cbranch_scc1 .LBB1_384
	s_add_i32 s35, s35, 1
	s_mov_b32 s37, s52
	s_mov_b32 s38, s39
	s_mov_b32 s47, s53
	s_branch .Lsc_row
